# GQA loop over the static LDS ring; tile-load addresses from one per-tile VALU add (32-bit lane offset + per-unit SGPR bases)
# speedup vs baseline: 1.0097x; 1.0097x over previous
; __device__ __forceinline__ unsigned cvt_pk_bf16(float lo, float hi) { unsigned r; asm volatile("v_cvt_pk_bf16_f32 %0, %1, %2" : "=v"(r) : "v"(lo), "v"(hi)); return r; }
; #define SWAIT() asm volatile("s_waitcnt vmcnt(2)" ::: "memory")
; template <int DQK, bool FIXM> ...
;     ...
;     const bf16_t* Qw = Qp + (size_t)(wid * 32 + r32) * ldq + hi * 8;
; #pragma unroll
;     for (int d0 = 0; d0 < NQ; ++d0) qr[d0] = *(const bf16x8*)(Qw + d0 * 16);
;     if constexpr (DQK == 96) { if (qtok0 >= 0) {
;         const int t = qtok0 + wid * 32 + r32, gr = t >> 6, gc = t & 63;
; #pragma unroll
;         for (int e = 0; e < 2; ++e) { const f32x2* tp = (e == 0) ? rope + gr * 8 + hi * 4 : rope + 2048 + gc * 8 + hi * 4;
;             const f32x4 cs0 = *(const f32x4*)tp, cs1 = *(const f32x4*)(tp + 2);
;             const u32x4 w = __builtin_bit_cast(u32x4, qr[4 + e]); u32x4 o;
;             { const float x1 = bf16lo(w.x), x2 = bf16hi(w.x); o.x = cvt_pk_bf16(x1 * cs0[0] - x2 * cs0[1], x1 * cs0[1] + x2 * cs0[0]); }
;             { const float x1 = bf16lo(w.y), x2 = bf16hi(w.y); o.y = cvt_pk_bf16(x1 * cs0[2] - x2 * cs0[3], x1 * cs0[3] + x2 * cs0[2]); }
;             { const float x1 = bf16lo(w.z), x2 = bf16hi(w.z); o.z = cvt_pk_bf16(x1 * cs1[0] - x2 * cs1[1], x1 * cs1[1] + x2 * cs1[0]); }
;             { const float x1 = bf16lo(w.w), x2 = bf16hi(w.w); o.w = cvt_pk_bf16(x1 * cs1[2] - x2 * cs1[3], x1 * cs1[3] + x2 * cs1[2]); }
;             qr[4 + e] = __builtin_bit_cast(bf16x8, o); } } }
;     const int sr = tid >> 3, c8 = tid & 7, sr2 = (tid >> 2) & 63, c4 = tid & 3;
;     const bool krw = (DQK == 96) && (tid < 256);
;     const int kn_st = B_KN + swz64(sr, c8), v_stw = B_V + v_st(sr, c8 * 8), kr_st = B_KR + swz32(sr2, c4);
;     const unsigned vb0 = (unsigned)(uintptr_t)lds + B_V + v_rd_base(lane);
;     bf16x8 skn[2], sv[2], skr[2];
;     ...
;     f32x16 pA0, pA1, pB0, pB1; float alA, alB; bf16x8 pa0, pa1, pa2, pa3;
;     int bV = 0, bK = BUF, bW = 2 * BUF;
;     ...
;     __syncthreads();
;     SLOAD(0, 0); asm volatile("s_waitcnt vmcnt(0)" ::: "memory"); SWRITE(0, 0);
;     SLOAD(1, 1); if (2 < NT) SLOAD(0, 2);
;     __syncthreads();
;     qkt<DQK>(pA0, pA1, lds, qr, r32, hi, negm);
;     if (FIXM) { alA = 1.f; _Pragma("unroll") for (int r = 0; r < 16; ++r) pA0[r] = __builtin_amdgcn_exp2f(pA0[r]); } else partialSM<true>(pA0, pA1, m_reg, negm, alA);
;     SWAIT(); SWRITEO(BUF, 1);
.LBB0_496:
	s_lshr_b32 s8, s8, 6
	s_and_b64 s[0:1], s[10:11], exec
	s_cselect_b32 s8, s8, s14
	s_and_b32 s9, s8, 7
	s_lshl_b64 s[0:1], s[4:5], 10
	s_add_u32 s0, s15, s0
	s_addc_u32 s1, s16, s1
	s_lshl_b32 s34, s9, 6
	s_lshl_b32 s9, s9, 7
	s_add_u32 s38, s0, s9
	s_addc_u32 s39, s1, 0
	s_lshl_b32 s0, s8, 5
	s_and_b32 s8, s0, 0x80
	s_add_u32 s0, s19, s8
	v_add_u32_e32 v16, s36, v1
	s_addc_u32 s1, s20, 0
	v_ashrrev_i32_e32 v17, 31, v16
	s_add_u32 s8, s23, s8
	v_lshl_add_u64 v[4:5], s[38:39], 0, v[192:193]
	v_lshlrev_b32_e32 v2, 1, v200
	v_lshlrev_b64 v[16:17], 8, v[16:17]
	s_addc_u32 s9, s24, 0
	v_lshl_add_u64 v[4:5], v[4:5], 0, v[2:3]
	v_lshl_add_u64 v[34:35], s[0:1], 0, v[16:17]
	v_lshlrev_b32_e32 v2, 1, v188
	v_lshl_add_u64 v[34:35], v[34:35], 0, v[2:3]
	v_lshl_add_u64 v[16:17], s[8:9], 0, v[16:17]
	global_load_dwordx4 v[114:117], v[4:5], off
	global_load_dwordx4 v[12:15], v[4:5], off offset:32
	global_load_dwordx4 v[8:11], v[4:5], off offset:64
	s_nop 0
	global_load_dwordx4 v[4:7], v[4:5], off offset:96
	s_barrier
	v_lshl_add_u64 v[16:17], v[16:17], 0, v[2:3]
	global_load_dwordx4 v[34:37], v[34:35], off
	s_nop 0
	global_load_dwordx4 v[38:41], v[16:17], off
	s_lshl_b32 s36, s31, 6
	s_sub_i32 s36, s29, s36
	s_and_b64 s[10:11], s[10:11], exec
	s_cselect_b32 s10, s12, s36
	v_add_u32_e32 v16, s10, v191
	v_ashrrev_i32_e32 v17, 31, v16
	v_lshlrev_b64 v[16:17], 8, v[16:17]
	v_add_u32_e32 v42, s10, v189
	v_lshl_add_u64 v[44:45], s[0:1], 0, v[16:17]
	v_lshl_add_u64 v[16:17], s[8:9], 0, v[16:17]
	s_waitcnt vmcnt(0)
	v_lshl_add_u64 v[44:45], v[44:45], 0, v[2:3]
	v_lshl_add_u64 v[16:17], v[16:17], 0, v[2:3]
	v_ashrrev_i32_e32 v43, 31, v42
	global_load_dwordx4 v[58:61], v[44:45], off
	global_load_dwordx4 v[62:65], v[16:17], off
	v_lshlrev_b64 v[16:17], 8, v[42:43]
	v_lshl_add_u64 v[42:43], s[0:1], 0, v[16:17]
	v_lshl_add_u64 v[16:17], s[8:9], 0, v[16:17]
	v_lshl_add_u64 v[42:43], v[42:43], 0, v[2:3]
	v_lshl_add_u64 v[16:17], v[16:17], 0, v[2:3]
	global_load_dwordx4 v[118:121], v[42:43], off
	global_load_dwordx4 v[122:125], v[16:17], off
	v_add_u32_e32 v106, 0, v187
	v_add_u32_e32 v46, v208, v209
	v_add_u32_e32 v107, 0, v214
	v_add_u32_e32 v16, v208, v210
	v_add_u32_e32 v17, v208, v211
	v_add_u32_e32 v57, v208, v212
	v_mov_b32_e32 v136, 0
	s_mov_b32 s10, 0xa000
	s_movk_i32 s11, 0x5000
	v_mov_b32_e32 v137, v221
	v_mov_b32_e32 v50, 0
	v_mov_b32_e32 v42, v136
	v_mov_b32_e32 v43, v136
	v_mov_b32_e32 v48, v136
	v_mov_b32_e32 v49, v136
	v_mov_b32_e32 v51, v136
	v_mov_b32_e32 v56, v136
	v_lshl_add_u64 v[134:135], s[8:9], 0, v[2:3]
	s_mov_b64 s[44:45], s[8:9]
	s_waitcnt vmcnt(5)
	ds_write_b128 v106, v[34:37]
	s_waitcnt vmcnt(4)
	ds_write_b128 v107, v[38:41] offset:12288
	s_waitcnt lgkmcnt(0)
	s_barrier
	ds_read_b128 v[34:37], v46
	ds_read_b128 v[38:41], v46 offset:4096
	s_waitcnt lgkmcnt(1)
	v_mfma_f32_32x32x16_bf16 v[82:97], v[34:37], v[114:117], v[18:33]
	ds_read_b128 v[34:37], v16
	ds_read_b128 v[44:47], v17
	ds_read_b128 v[52:55], v17 offset:4096
	ds_read_b128 v[98:101], v57
	ds_read_b128 v[102:105], v57 offset:4096
	v_mov_b32_e32 v57, v136
	s_waitcnt lgkmcnt(5)
	v_mfma_f32_32x32x16_bf16 v[66:81], v[38:41], v[114:117], v[18:33]
	ds_read_b128 v[38:41], v16 offset:4096
	s_waitcnt vmcnt(2)
	v_lshl_add_u64 v[16:17], s[0:1], 0, v[2:3]
	s_mov_b64 s[42:43], s[0:1]
	s_add_i32 s0, s30, -1
	s_waitcnt vmcnt(3)
	ds_write_b128 v106, v[58:61] offset:20480
	s_waitcnt vmcnt(2)
	ds_write_b128 v107, v[62:65] offset:32768
	v_mov_b32_e32 v58, v136
	v_mov_b32_e32 v59, v136
	s_waitcnt lgkmcnt(7)
	v_mfma_f32_32x32x16_bf16 v[82:97], v[34:37], v[12:15], v[82:97]
	v_mov_b32_e32 v34, 0
	v_mov_b32_e32 v35, v136
	v_mov_b32_e32 v36, v136
	v_mov_b32_e32 v37, v136
	v_mov_b32_e32 v60, v136
	v_mov_b32_e32 v61, v136
	v_mov_b32_e32 v62, v136
	s_waitcnt lgkmcnt(2)
	v_mfma_f32_32x32x16_bf16 v[66:81], v[38:41], v[12:15], v[66:81]
	v_mov_b32_e32 v38, v136
	v_mov_b32_e32 v39, v136
	v_mov_b32_e32 v40, v136
	v_mov_b32_e32 v41, v136
	v_mov_b32_e32 v63, v136
	v_mov_b32_e32 v64, v136
	v_mov_b32_e32 v65, v136
	v_mfma_f32_32x32x16_bf16 v[82:97], v[44:47], v[8:11], v[82:97]
	v_mov_b32_e32 v44, v136
	v_mov_b32_e32 v45, v136
	v_mov_b32_e32 v46, v136
	v_mov_b32_e32 v47, v136
	v_mfma_f32_32x32x16_bf16 v[66:81], v[52:55], v[8:11], v[66:81]
	v_mov_b32_e32 v52, v136
	v_mov_b32_e32 v53, v136
	v_mov_b32_e32 v54, v136
	v_mov_b32_e32 v55, v136
	v_mfma_f32_32x32x16_bf16 v[82:97], v[98:101], v[4:7], v[82:97]
	v_mfma_f32_32x32x16_bf16 v[66:81], v[102:105], v[4:7], v[66:81]
	s_nop 10
	v_exp_f32_e32 v143, v82
	v_exp_f32_e32 v145, v83
	v_exp_f32_e32 v141, v84
	v_exp_f32_e32 v144, v85
	v_exp_f32_e32 v139, v86
	v_exp_f32_e32 v142, v87
	v_exp_f32_e32 v138, v88
	v_exp_f32_e32 v140, v89
	v_exp_f32_e32 v151, v90
	v_exp_f32_e32 v153, v91
	v_exp_f32_e32 v149, v92
	v_exp_f32_e32 v152, v93
	v_exp_f32_e32 v147, v94
	v_exp_f32_e32 v150, v95
	v_exp_f32_e32 v146, v96
	v_exp_f32_e32 v148, v97
	v_add_u32_e32 v223, v208, v209
	v_add_u32_e32 v252, v208, v210
	v_add_u32_e32 v253, v208, v211
	v_lshlrev_b32_e32 v137, 8, v221
	v_add_u32_e32 v137, v137, v2
	v_add_u32_e32 v2, v208, v212
; #define LAS __attribute__((address_space(3)))
; __device__ __forceinline__ void finishSM(f32x16& p0, f32x16& p1, float alpha, float& l_reg, bf16x8& pa0, bf16x8& pa1, bf16x8& pa2, bf16x8& pa3) {
; #pragma unroll
;     for (int r = 0; r < 16; ++r) p1[r] = EXP_PROBE ? fmaf(p1[r], 0.001f, 1.f) : __builtin_amdgcn_exp2f(p1[r]);
;     float ps = 0.f;
; #pragma unroll
;     for (int r = 0; r < 16; ++r) ps += p0[r];
; #pragma unroll
;     for (int r = 0; r < 16; ++r) ps += p1[r];
;     { auto rr = __builtin_amdgcn_permlane32_swap(__float_as_uint(ps), __float_as_uint(ps), false, false);
;       ps = __uint_as_float(rr[0]) + __uint_as_float(rr[1]); }
;     l_reg = l_reg * alpha + ps;
;     ATT_PKN(p0, 0, pa0); ATT_PKN(p0, 8, pa1); ATT_PKN(p1, 0, pa2); ATT_PKN(p1, 8, pa3);
; }
; template <int DQK> __device__ __forceinline__ void qkt(f32x16& p0, f32x16& p1, const LAS char* buf, const bf16x8* qr, int r32, int hi, const f32x16& negm) {
; #pragma unroll
;     for (int d0 = 0; d0 < 4; ++d0) { const int ch = d0 * 2 + hi;
;         const bf16x8 b0 = *(const LAS bf16x8*)(buf + B_KN + swz64(r32, ch));
;         const bf16x8 b1 = *(const LAS bf16x8*)(buf + B_KN + swz64(32 + r32, ch));
;         p0 = __builtin_amdgcn_mfma_f32_32x32x16_bf16(b0, qr[d0], d0 == 0 ? negm : p0, 0, 0, 0);
;         p1 = __builtin_amdgcn_mfma_f32_32x32x16_bf16(b1, qr[d0], d0 == 0 ? negm : p1, 0, 0, 0); }
; template <bool FIXM> __device__ __forceinline__ void pv_psm(f32x16& o0, f32x16& o1, unsigned vb, bf16x8 pa0, bf16x8 pa1, bf16x8 pa2, bf16x8 pa3,
;                                        f32x16& p0, f32x16& p1, float& m_reg, f32x16& negm, float& alpha) {
;     { const s16x4 l0 = tr_read<v_rd_off(0, 0, 0)>(vb), h0 = tr_read<v_rd_off(0, 0, 1)>(vb), l1 = tr_read<v_rd_off(0, 1, 0)>(vb), h1 = tr_read<v_rd_off(0, 1, 1)>(vb);
;       const s16x4 l2 = tr_read<v_rd_off(0, 2, 0)>(vb), h2 = tr_read<v_rd_off(0, 2, 1)>(vb), l3 = tr_read<v_rd_off(0, 3, 0)>(vb), h3 = tr_read<v_rd_off(0, 3, 1)>(vb);
;       float pmax = 0.f; SBAR(); if (!FIXM) pmax = psm_max(p0, p1); else { _Pragma("unroll") for (int r = 0; r < 8; ++r) p0[r] = __builtin_amdgcn_exp2f(p0[r]); } SBAR();
;       asm volatile("s_waitcnt lgkmcnt(0)" ::: "memory"); SBAR();
;       o0 = __builtin_amdgcn_mfma_f32_32x32x16_bf16(ATT_PK(l0, h0), pa0, o0, 0, 0, 0);
;       o0 = __builtin_amdgcn_mfma_f32_32x32x16_bf16(ATT_PK(l1, h1), pa1, o0, 0, 0, 0);
.LBB0_497:
	s_waitcnt lgkmcnt(0)
	s_barrier
	ds_read_b128 v[224:227], v223 offset:20480
	ds_read_b128 v[228:231], v223 offset:24576
	ds_read_b128 v[232:235], v252 offset:20480
	ds_read_b128 v[236:239], v252 offset:24576
	ds_read_b128 v[240:243], v253 offset:20480
	ds_read_b128 v[244:247], v253 offset:24576
	ds_read_b128 v[248:251], v2 offset:20480
	v_exp_f32_e32 v66, v66
	v_exp_f32_e32 v67, v67
	v_exp_f32_e32 v68, v68
	v_exp_f32_e32 v69, v69
	v_exp_f32_e32 v70, v70
	v_exp_f32_e32 v71, v71
	v_exp_f32_e32 v72, v72
	v_exp_f32_e32 v73, v73
	s_waitcnt lgkmcnt(6)
	v_mfma_f32_32x32x16_bf16 v[98:113], v[224:227], v[114:117], v[18:33]
	ds_read_b128 v[224:227], v2 offset:24576
	v_exp_f32_e32 v74, v74
	v_exp_f32_e32 v75, v75
	v_exp_f32_e32 v76, v76
	v_cvt_pk_bf16_f32 v156, v143, v145
	v_cvt_pk_bf16_f32 v157, v141, v144
	v_add_f32_e32 v164, 0, v143
	v_add_f32_e32 v164, v145, v164
	v_add_f32_e32 v164, v141, v164
	s_waitcnt lgkmcnt(6)
	v_mfma_f32_32x32x16_bf16 v[82:97], v[228:231], v[114:117], v[18:33]
	v_exp_f32_e32 v77, v77
	v_exp_f32_e32 v78, v78
	v_exp_f32_e32 v79, v79
	v_cvt_pk_bf16_f32 v158, v139, v142
	v_cvt_pk_bf16_f32 v159, v138, v140
	v_add_f32_e32 v164, v144, v164
	v_add_f32_e32 v164, v139, v164
	v_add_f32_e32 v164, v142, v164
	s_waitcnt lgkmcnt(5)
	v_mfma_f32_32x32x16_bf16 v[98:113], v[232:235], v[12:15], v[98:113]
	v_exp_f32_e32 v80, v80
	v_exp_f32_e32 v81, v81
	v_cvt_pk_bf16_f32 v160, v151, v153
	v_cvt_pk_bf16_f32 v161, v149, v152
	v_cvt_pk_bf16_f32 v162, v147, v150
	v_cvt_pk_bf16_f32 v163, v146, v148
	v_add_f32_e32 v164, v138, v164
	v_add_f32_e32 v164, v140, v164
	v_add_f32_e32 v164, v151, v164
	s_waitcnt lgkmcnt(4)
	v_mfma_f32_32x32x16_bf16 v[82:97], v[236:239], v[12:15], v[82:97]
	v_add_f32_e32 v164, v153, v164
	v_add_f32_e32 v164, v149, v164
	v_add_f32_e32 v164, v152, v164
	v_add_f32_e32 v164, v147, v164
	v_add_f32_e32 v164, v150, v164
	v_add_f32_e32 v164, v146, v164
	v_add_f32_e32 v164, v148, v164
	s_waitcnt lgkmcnt(3)
	v_mfma_f32_32x32x16_bf16 v[98:113], v[240:243], v[8:11], v[98:113]
	ds_read_b64_tr_b16 v[138:139], v213 offset:0
	ds_read_b64_tr_b16 v[140:141], v213 offset:1024
	ds_read_b64_tr_b16 v[142:143], v213 offset:2048
	ds_read_b64_tr_b16 v[144:145], v213 offset:3072
	v_add_f32_e32 v164, v66, v164
	v_add_f32_e32 v164, v67, v164
	v_add_f32_e32 v164, v68, v164
	v_add_f32_e32 v164, v69, v164
	s_waitcnt lgkmcnt(6)
	v_mfma_f32_32x32x16_bf16 v[82:97], v[244:247], v[8:11], v[82:97]
	ds_read_b64_tr_b16 v[146:147], v213 offset:4096
	ds_read_b64_tr_b16 v[148:149], v213 offset:5120
	ds_read_b64_tr_b16 v[150:151], v213 offset:6144
	ds_read_b64_tr_b16 v[152:153], v213 offset:7168
	v_add_f32_e32 v164, v70, v164
	v_add_f32_e32 v164, v71, v164
	v_add_f32_e32 v164, v72, v164
	v_add_f32_e32 v164, v73, v164
	s_waitcnt lgkmcnt(9)
	v_mfma_f32_32x32x16_bf16 v[98:113], v[248:251], v[4:7], v[98:113]
	v_add_f32_e32 v164, v74, v164
	v_add_f32_e32 v164, v75, v164
	v_add_f32_e32 v164, v76, v164
	v_add_f32_e32 v164, v77, v164
	s_waitcnt lgkmcnt(8)
	v_mfma_f32_32x32x16_bf16 v[82:97], v[224:227], v[4:7], v[82:97]
	ds_read_b64_tr_b16 v[224:225], v213 offset:512
	ds_read_b64_tr_b16 v[226:227], v213 offset:1536
	ds_read_b64_tr_b16 v[228:229], v213 offset:2560
	ds_read_b64_tr_b16 v[230:231], v213 offset:3584
	ds_read_b64_tr_b16 v[232:233], v213 offset:4608
	ds_read_b64_tr_b16 v[234:235], v213 offset:5632
	ds_read_b64_tr_b16 v[236:237], v213 offset:6656
	ds_read_b64_tr_b16 v[238:239], v213 offset:7680
	s_waitcnt lgkmcnt(8)
	v_mfma_f32_32x32x16_bf16 v[50:65], v[138:141], v[156:159], v[50:65]
	v_add_f32_e32 v164, v78, v164
	v_add_f32_e32 v164, v79, v164
	v_add_f32_e32 v164, v80, v164
	v_add_f32_e32 v154, v81, v164
	v_mov_b32_e32 v155, v154
	v_mfma_f32_32x32x16_bf16 v[50:65], v[142:145], v[160:163], v[50:65]
	v_cvt_pk_bf16_f32 v66, v66, v67
	v_cvt_pk_bf16_f32 v67, v68, v69
	v_cvt_pk_bf16_f32 v68, v70, v71
	v_cvt_pk_bf16_f32 v69, v72, v73
	v_cvt_pk_bf16_f32 v70, v74, v75
	v_cvt_pk_bf16_f32 v71, v76, v77
	v_cvt_pk_bf16_f32 v72, v78, v79
	v_cvt_pk_bf16_f32 v73, v80, v81
	v_permlane32_swap_b32_e32 v154, v155
	v_mfma_f32_32x32x16_bf16 v[50:65], v[146:149], v[66:69], v[50:65]
	s_add_i32 s8, s13, -1
	s_cmp_lt_u32 s8, s31
	s_cselect_b32 s9, 0, s31
	s_cselect_b32 s35, s12, s29
	s_lshl_b32 s9, s9, 6
	s_sub_i32 s9, s35, s9
	s_lshl_b32 s52, s9, 8
	s_add_i32 s52, s52, -16384
	v_mfma_f32_32x32x16_bf16 v[50:65], v[150:153], v[70:73], v[50:65]
	v_add_u32_e32 v126, s52, v137
	global_load_dwordx4 v[130:133], v126, s[42:43]
	global_load_dwordx4 v[126:129], v126, s[44:45]
	s_waitcnt lgkmcnt(0)
	v_mfma_f32_32x32x16_bf16 v[34:49], v[224:227], v[156:159], v[34:49]
	s_waitcnt vmcnt(2)
	ds_write_b128 v187, v[118:121] offset:40960
	ds_write_b128 v214, v[122:125] offset:53248
	v_exp_f32_e32 v168, v98
	v_exp_f32_e32 v169, v99
	v_mfma_f32_32x32x16_bf16 v[34:49], v[228:231], v[160:163], v[34:49]
	v_exp_f32_e32 v170, v100
	v_exp_f32_e32 v171, v101
	v_exp_f32_e32 v172, v102
	v_exp_f32_e32 v173, v103
	v_mfma_f32_32x32x16_bf16 v[34:49], v[232:235], v[66:69], v[34:49]
	v_exp_f32_e32 v174, v104
	v_exp_f32_e32 v175, v105
	v_exp_f32_e32 v176, v106
	v_exp_f32_e32 v177, v107
	v_exp_f32_e32 v178, v108
	v_mfma_f32_32x32x16_bf16 v[34:49], v[236:239], v[70:73], v[34:49]
	v_exp_f32_e32 v179, v109
	v_exp_f32_e32 v180, v110
	v_exp_f32_e32 v181, v111
	v_exp_f32_e32 v182, v112
	v_exp_f32_e32 v183, v113
	s_waitcnt lgkmcnt(0)
	s_barrier
; #define LAS __attribute__((address_space(3)))
; __device__ __forceinline__ void finishSM(f32x16& p0, f32x16& p1, float alpha, float& l_reg, bf16x8& pa0, bf16x8& pa1, bf16x8& pa2, bf16x8& pa3) {
; #pragma unroll
;     for (int r = 0; r < 16; ++r) p1[r] = EXP_PROBE ? fmaf(p1[r], 0.001f, 1.f) : __builtin_amdgcn_exp2f(p1[r]);
;     float ps = 0.f;
; #pragma unroll
;     for (int r = 0; r < 16; ++r) ps += p0[r];
; #pragma unroll
;     for (int r = 0; r < 16; ++r) ps += p1[r];
;     { auto rr = __builtin_amdgcn_permlane32_swap(__float_as_uint(ps), __float_as_uint(ps), false, false);
;       ps = __uint_as_float(rr[0]) + __uint_as_float(rr[1]); }
;     l_reg = l_reg * alpha + ps;
;     ATT_PKN(p0, 0, pa0); ATT_PKN(p0, 8, pa1); ATT_PKN(p1, 0, pa2); ATT_PKN(p1, 8, pa3);
; }
; template <int DQK> __device__ __forceinline__ void qkt(f32x16& p0, f32x16& p1, const LAS char* buf, const bf16x8* qr, int r32, int hi, const f32x16& negm) {
; #pragma unroll
;     for (int d0 = 0; d0 < 4; ++d0) { const int ch = d0 * 2 + hi;
;         const bf16x8 b0 = *(const LAS bf16x8*)(buf + B_KN + swz64(r32, ch));
;         const bf16x8 b1 = *(const LAS bf16x8*)(buf + B_KN + swz64(32 + r32, ch));
;         p0 = __builtin_amdgcn_mfma_f32_32x32x16_bf16(b0, qr[d0], d0 == 0 ? negm : p0, 0, 0, 0);
;         p1 = __builtin_amdgcn_mfma_f32_32x32x16_bf16(b1, qr[d0], d0 == 0 ? negm : p1, 0, 0, 0); }
; template <bool FIXM> __device__ __forceinline__ void pv_psm(f32x16& o0, f32x16& o1, unsigned vb, bf16x8 pa0, bf16x8 pa1, bf16x8 pa2, bf16x8 pa3,
;                                        f32x16& p0, f32x16& p1, float& m_reg, f32x16& negm, float& alpha) {
;     { const s16x4 l0 = tr_read<v_rd_off(0, 0, 0)>(vb), h0 = tr_read<v_rd_off(0, 0, 1)>(vb), l1 = tr_read<v_rd_off(0, 1, 0)>(vb), h1 = tr_read<v_rd_off(0, 1, 1)>(vb);
;       const s16x4 l2 = tr_read<v_rd_off(0, 2, 0)>(vb), h2 = tr_read<v_rd_off(0, 2, 1)>(vb), l3 = tr_read<v_rd_off(0, 3, 0)>(vb), h3 = tr_read<v_rd_off(0, 3, 1)>(vb);
;       float pmax = 0.f; SBAR(); if (!FIXM) pmax = psm_max(p0, p1); else { _Pragma("unroll") for (int r = 0; r < 8; ++r) p0[r] = __builtin_amdgcn_exp2f(p0[r]); } SBAR();
;       asm volatile("s_waitcnt lgkmcnt(0)" ::: "memory"); SBAR();
;       o0 = __builtin_amdgcn_mfma_f32_32x32x16_bf16(ATT_PK(l0, h0), pa0, o0, 0, 0, 0);
;       o0 = __builtin_amdgcn_mfma_f32_32x32x16_bf16(ATT_PK(l1, h1), pa1, o0, 0, 0, 0);
	ds_read_b128 v[224:227], v223 offset:40960
	ds_read_b128 v[228:231], v223 offset:45056
	ds_read_b128 v[232:235], v252 offset:40960
	ds_read_b128 v[236:239], v252 offset:45056
	ds_read_b128 v[240:243], v253 offset:40960
	ds_read_b128 v[244:247], v253 offset:45056
	ds_read_b128 v[248:251], v2 offset:40960
	v_exp_f32_e32 v82, v82
	v_exp_f32_e32 v83, v83
	v_exp_f32_e32 v84, v84
	v_exp_f32_e32 v85, v85
	v_exp_f32_e32 v86, v86
	v_exp_f32_e32 v87, v87
	v_exp_f32_e32 v88, v88
	v_exp_f32_e32 v89, v89
	s_waitcnt lgkmcnt(6)
	v_mfma_f32_32x32x16_bf16 v[98:113], v[224:227], v[114:117], v[18:33]
	ds_read_b128 v[224:227], v2 offset:45056
	v_exp_f32_e32 v90, v90
	v_exp_f32_e32 v91, v91
	v_exp_f32_e32 v92, v92
	v_cvt_pk_bf16_f32 v156, v168, v169
	v_cvt_pk_bf16_f32 v157, v170, v171
	v_add_f32_e32 v164, 0, v168
	v_add_f32_e32 v164, v169, v164
	v_add_f32_e32 v164, v170, v164
	s_waitcnt lgkmcnt(6)
	v_mfma_f32_32x32x16_bf16 v[66:81], v[228:231], v[114:117], v[18:33]
	v_exp_f32_e32 v93, v93
	v_exp_f32_e32 v94, v94
	v_exp_f32_e32 v95, v95
	v_cvt_pk_bf16_f32 v158, v172, v173
	v_cvt_pk_bf16_f32 v159, v174, v175
	v_add_f32_e32 v164, v171, v164
	v_add_f32_e32 v164, v172, v164
	v_add_f32_e32 v164, v173, v164
	s_waitcnt lgkmcnt(5)
	v_mfma_f32_32x32x16_bf16 v[98:113], v[232:235], v[12:15], v[98:113]
	v_exp_f32_e32 v96, v96
	v_exp_f32_e32 v97, v97
	v_cvt_pk_bf16_f32 v160, v176, v177
	v_cvt_pk_bf16_f32 v161, v178, v179
	v_cvt_pk_bf16_f32 v162, v180, v181
	v_cvt_pk_bf16_f32 v163, v182, v183
	v_add_f32_e32 v164, v174, v164
	v_add_f32_e32 v164, v175, v164
	v_add_f32_e32 v164, v176, v164
	s_waitcnt lgkmcnt(4)
	v_mfma_f32_32x32x16_bf16 v[66:81], v[236:239], v[12:15], v[66:81]
	v_add_f32_e32 v164, v177, v164
	v_add_f32_e32 v164, v178, v164
	v_add_f32_e32 v164, v179, v164
	v_add_f32_e32 v164, v180, v164
	v_add_f32_e32 v164, v181, v164
	v_add_f32_e32 v164, v182, v164
	v_add_f32_e32 v164, v183, v164
	s_waitcnt lgkmcnt(3)
	v_mfma_f32_32x32x16_bf16 v[98:113], v[240:243], v[8:11], v[98:113]
	ds_read_b64_tr_b16 v[168:169], v213 offset:20480
	ds_read_b64_tr_b16 v[170:171], v213 offset:21504
	ds_read_b64_tr_b16 v[172:173], v213 offset:22528
	ds_read_b64_tr_b16 v[174:175], v213 offset:23552
	v_add_f32_e32 v164, v82, v164
	v_add_f32_e32 v164, v83, v164
	v_add_f32_e32 v164, v84, v164
	v_add_f32_e32 v164, v85, v164
	s_waitcnt lgkmcnt(6)
	v_mfma_f32_32x32x16_bf16 v[66:81], v[244:247], v[8:11], v[66:81]
	ds_read_b64_tr_b16 v[176:177], v213 offset:24576
	ds_read_b64_tr_b16 v[178:179], v213 offset:25600
	ds_read_b64_tr_b16 v[180:181], v213 offset:26624
	ds_read_b64_tr_b16 v[182:183], v213 offset:27648
	v_add_f32_e32 v164, v86, v164
	v_add_f32_e32 v164, v87, v164
	v_add_f32_e32 v164, v88, v164
	v_add_f32_e32 v164, v89, v164
	s_waitcnt lgkmcnt(9)
	v_mfma_f32_32x32x16_bf16 v[98:113], v[248:251], v[4:7], v[98:113]
	v_add_f32_e32 v164, v90, v164
	v_add_f32_e32 v164, v91, v164
	v_add_f32_e32 v164, v92, v164
	v_add_f32_e32 v164, v93, v164
	s_waitcnt lgkmcnt(8)
	v_mfma_f32_32x32x16_bf16 v[66:81], v[224:227], v[4:7], v[66:81]
	ds_read_b64_tr_b16 v[224:225], v213 offset:20992
	ds_read_b64_tr_b16 v[226:227], v213 offset:22016
	ds_read_b64_tr_b16 v[228:229], v213 offset:23040
	ds_read_b64_tr_b16 v[230:231], v213 offset:24064
	ds_read_b64_tr_b16 v[232:233], v213 offset:25088
	ds_read_b64_tr_b16 v[234:235], v213 offset:26112
	ds_read_b64_tr_b16 v[236:237], v213 offset:27136
	ds_read_b64_tr_b16 v[238:239], v213 offset:28160
	s_waitcnt lgkmcnt(8)
	v_mfma_f32_32x32x16_bf16 v[50:65], v[168:171], v[156:159], v[50:65]
	v_add_f32_e32 v164, v94, v164
	v_add_f32_e32 v164, v95, v164
	v_add_f32_e32 v164, v96, v164
	v_add_f32_e32 v164, v97, v164
	v_mov_b32_e32 v165, v164
	v_mfma_f32_32x32x16_bf16 v[50:65], v[172:175], v[160:163], v[50:65]
	v_cvt_pk_bf16_f32 v82, v82, v83
	v_cvt_pk_bf16_f32 v83, v84, v85
	v_cvt_pk_bf16_f32 v84, v86, v87
	v_cvt_pk_bf16_f32 v85, v88, v89
	v_cvt_pk_bf16_f32 v86, v90, v91
	v_cvt_pk_bf16_f32 v87, v92, v93
	v_cvt_pk_bf16_f32 v88, v94, v95
	v_cvt_pk_bf16_f32 v89, v96, v97
	v_permlane32_swap_b32_e32 v164, v165
	v_mfma_f32_32x32x16_bf16 v[50:65], v[176:179], v[82:85], v[50:65]
	v_mfma_f32_32x32x16_bf16 v[50:65], v[180:183], v[86:89], v[50:65]
	s_cmp_ge_u32 s13, s30
	s_cbranch_scc1 .Lgqa_b_noload_0
	s_cmp_lt_u32 s13, s31
	s_cselect_b32 s9, 0, s31
	s_cselect_b32 s35, s12, s29
	s_lshl_b32 s9, s9, 6
	s_sub_i32 s9, s35, s9
	s_lshl_b32 s52, s9, 8
	v_add_u32_e32 v122, s52, v137
	global_load_dwordx4 v[118:121], v122, s[42:43]
	global_load_dwordx4 v[122:125], v122, s[44:45]
; #define LAS __attribute__((address_space(3)))
; __device__ __forceinline__ void finishSM(f32x16& p0, f32x16& p1, float alpha, float& l_reg, bf16x8& pa0, bf16x8& pa1, bf16x8& pa2, bf16x8& pa3) {
; #pragma unroll
;     for (int r = 0; r < 16; ++r) p1[r] = EXP_PROBE ? fmaf(p1[r], 0.001f, 1.f) : __builtin_amdgcn_exp2f(p1[r]);
;     float ps = 0.f;
; #pragma unroll
;     for (int r = 0; r < 16; ++r) ps += p0[r];
; #pragma unroll
;     for (int r = 0; r < 16; ++r) ps += p1[r];
;     { auto rr = __builtin_amdgcn_permlane32_swap(__float_as_uint(ps), __float_as_uint(ps), false, false);
;       ps = __uint_as_float(rr[0]) + __uint_as_float(rr[1]); }
;     l_reg = l_reg * alpha + ps;
;     ATT_PKN(p0, 0, pa0); ATT_PKN(p0, 8, pa1); ATT_PKN(p1, 0, pa2); ATT_PKN(p1, 8, pa3);
; }
; template <int DQK> __device__ __forceinline__ void qkt(f32x16& p0, f32x16& p1, const LAS char* buf, const bf16x8* qr, int r32, int hi, const f32x16& negm) {
; #pragma unroll
;     for (int d0 = 0; d0 < 4; ++d0) { const int ch = d0 * 2 + hi;
;         const bf16x8 b0 = *(const LAS bf16x8*)(buf + B_KN + swz64(r32, ch));
;         const bf16x8 b1 = *(const LAS bf16x8*)(buf + B_KN + swz64(32 + r32, ch));
;         p0 = __builtin_amdgcn_mfma_f32_32x32x16_bf16(b0, qr[d0], d0 == 0 ? negm : p0, 0, 0, 0);
;         p1 = __builtin_amdgcn_mfma_f32_32x32x16_bf16(b1, qr[d0], d0 == 0 ? negm : p1, 0, 0, 0); }
; template <bool FIXM> __device__ __forceinline__ void pv_psm(f32x16& o0, f32x16& o1, unsigned vb, bf16x8 pa0, bf16x8 pa1, bf16x8 pa2, bf16x8 pa3,
;                                        f32x16& p0, f32x16& p1, float& m_reg, f32x16& negm, float& alpha) {
;     { const s16x4 l0 = tr_read<v_rd_off(0, 0, 0)>(vb), h0 = tr_read<v_rd_off(0, 0, 1)>(vb), l1 = tr_read<v_rd_off(0, 1, 0)>(vb), h1 = tr_read<v_rd_off(0, 1, 1)>(vb);
;       const s16x4 l2 = tr_read<v_rd_off(0, 2, 0)>(vb), h2 = tr_read<v_rd_off(0, 2, 1)>(vb), l3 = tr_read<v_rd_off(0, 3, 0)>(vb), h3 = tr_read<v_rd_off(0, 3, 1)>(vb);
;       float pmax = 0.f; SBAR(); if (!FIXM) pmax = psm_max(p0, p1); else { _Pragma("unroll") for (int r = 0; r < 8; ++r) p0[r] = __builtin_amdgcn_exp2f(p0[r]); } SBAR();
;       asm volatile("s_waitcnt lgkmcnt(0)" ::: "memory"); SBAR();
;       o0 = __builtin_amdgcn_mfma_f32_32x32x16_bf16(ATT_PK(l0, h0), pa0, o0, 0, 0, 0);
;       o0 = __builtin_amdgcn_mfma_f32_32x32x16_bf16(ATT_PK(l1, h1), pa1, o0, 0, 0, 0);
.Lgqa_b_ld_done_0:
	s_waitcnt lgkmcnt(0)
	v_mfma_f32_32x32x16_bf16 v[34:49], v[224:227], v[156:159], v[34:49]
	s_waitcnt vmcnt(2)
	ds_write_b128 v187, v[130:133] offset:0
	ds_write_b128 v214, v[126:129] offset:12288
	v_exp_f32_e32 v143, v98
	v_exp_f32_e32 v145, v99
	v_mfma_f32_32x32x16_bf16 v[34:49], v[228:231], v[160:163], v[34:49]
	v_exp_f32_e32 v141, v100
	v_exp_f32_e32 v144, v101
	v_exp_f32_e32 v139, v102
	v_exp_f32_e32 v142, v103
	v_mfma_f32_32x32x16_bf16 v[34:49], v[232:235], v[82:85], v[34:49]
	v_exp_f32_e32 v138, v104
	v_exp_f32_e32 v140, v105
	v_exp_f32_e32 v151, v106
	v_exp_f32_e32 v153, v107
	v_exp_f32_e32 v149, v108
	v_mfma_f32_32x32x16_bf16 v[34:49], v[236:239], v[86:89], v[34:49]
	v_exp_f32_e32 v152, v109
	v_exp_f32_e32 v147, v110
	v_exp_f32_e32 v150, v111
	v_exp_f32_e32 v146, v112
	v_exp_f32_e32 v148, v113
	v_add_f32_e32 v154, v154, v155
	v_add_f32_e32 v136, v136, v154
	v_add_f32_e32 v164, v164, v165
	v_add_f32_e32 v136, v136, v164
	s_add_i32 s13, s13, 2
	v_add_u32_e32 v137, 0x8000, v137
	s_cmp_lt_u32 s8, s0
	s_cbranch_scc0 .Lgqa_exit_0
	s_waitcnt lgkmcnt(0)
	s_barrier
	ds_read_b128 v[224:227], v223 offset:0
	ds_read_b128 v[228:231], v223 offset:4096
	ds_read_b128 v[232:235], v252 offset:0
	ds_read_b128 v[236:239], v252 offset:4096
	ds_read_b128 v[240:243], v253 offset:0
	ds_read_b128 v[244:247], v253 offset:4096
	ds_read_b128 v[248:251], v2 offset:0
	v_exp_f32_e32 v66, v66
	v_exp_f32_e32 v67, v67
	v_exp_f32_e32 v68, v68
	v_exp_f32_e32 v69, v69
	v_exp_f32_e32 v70, v70
	v_exp_f32_e32 v71, v71
	v_exp_f32_e32 v72, v72
	v_exp_f32_e32 v73, v73
	s_waitcnt lgkmcnt(6)
	v_mfma_f32_32x32x16_bf16 v[98:113], v[224:227], v[114:117], v[18:33]
	ds_read_b128 v[224:227], v2 offset:4096
	v_exp_f32_e32 v74, v74
	v_exp_f32_e32 v75, v75
	v_exp_f32_e32 v76, v76
	v_cvt_pk_bf16_f32 v156, v143, v145
	v_cvt_pk_bf16_f32 v157, v141, v144
	v_add_f32_e32 v164, 0, v143
	v_add_f32_e32 v164, v145, v164
	v_add_f32_e32 v164, v141, v164
	s_waitcnt lgkmcnt(6)
	v_mfma_f32_32x32x16_bf16 v[82:97], v[228:231], v[114:117], v[18:33]
	v_exp_f32_e32 v77, v77
	v_exp_f32_e32 v78, v78
	v_exp_f32_e32 v79, v79
	v_cvt_pk_bf16_f32 v158, v139, v142
	v_cvt_pk_bf16_f32 v159, v138, v140
	v_add_f32_e32 v164, v144, v164
	v_add_f32_e32 v164, v139, v164
	v_add_f32_e32 v164, v142, v164
	s_waitcnt lgkmcnt(5)
	v_mfma_f32_32x32x16_bf16 v[98:113], v[232:235], v[12:15], v[98:113]
	v_exp_f32_e32 v80, v80
	v_exp_f32_e32 v81, v81
	v_cvt_pk_bf16_f32 v160, v151, v153
	v_cvt_pk_bf16_f32 v161, v149, v152
	v_cvt_pk_bf16_f32 v162, v147, v150
	v_cvt_pk_bf16_f32 v163, v146, v148
	v_add_f32_e32 v164, v138, v164
	v_add_f32_e32 v164, v140, v164
	v_add_f32_e32 v164, v151, v164
	s_waitcnt lgkmcnt(4)
	v_mfma_f32_32x32x16_bf16 v[82:97], v[236:239], v[12:15], v[82:97]
	v_add_f32_e32 v164, v153, v164
	v_add_f32_e32 v164, v149, v164
	v_add_f32_e32 v164, v152, v164
	v_add_f32_e32 v164, v147, v164
	v_add_f32_e32 v164, v150, v164
	v_add_f32_e32 v164, v146, v164
	v_add_f32_e32 v164, v148, v164
	s_waitcnt lgkmcnt(3)
	v_mfma_f32_32x32x16_bf16 v[98:113], v[240:243], v[8:11], v[98:113]
	ds_read_b64_tr_b16 v[138:139], v213 offset:40960
	ds_read_b64_tr_b16 v[140:141], v213 offset:41984
	ds_read_b64_tr_b16 v[142:143], v213 offset:43008
	ds_read_b64_tr_b16 v[144:145], v213 offset:44032
	v_add_f32_e32 v164, v66, v164
	v_add_f32_e32 v164, v67, v164
	v_add_f32_e32 v164, v68, v164
	v_add_f32_e32 v164, v69, v164
	s_waitcnt lgkmcnt(6)
	v_mfma_f32_32x32x16_bf16 v[82:97], v[244:247], v[8:11], v[82:97]
	ds_read_b64_tr_b16 v[146:147], v213 offset:45056
	ds_read_b64_tr_b16 v[148:149], v213 offset:46080
	ds_read_b64_tr_b16 v[150:151], v213 offset:47104
	ds_read_b64_tr_b16 v[152:153], v213 offset:48128
	v_add_f32_e32 v164, v70, v164
	v_add_f32_e32 v164, v71, v164
	v_add_f32_e32 v164, v72, v164
	v_add_f32_e32 v164, v73, v164
	s_waitcnt lgkmcnt(9)
	v_mfma_f32_32x32x16_bf16 v[98:113], v[248:251], v[4:7], v[98:113]
	v_add_f32_e32 v164, v74, v164
	v_add_f32_e32 v164, v75, v164
	v_add_f32_e32 v164, v76, v164
	v_add_f32_e32 v164, v77, v164
	s_waitcnt lgkmcnt(8)
	v_mfma_f32_32x32x16_bf16 v[82:97], v[224:227], v[4:7], v[82:97]
	ds_read_b64_tr_b16 v[224:225], v213 offset:41472
	ds_read_b64_tr_b16 v[226:227], v213 offset:42496
	ds_read_b64_tr_b16 v[228:229], v213 offset:43520
	ds_read_b64_tr_b16 v[230:231], v213 offset:44544
	ds_read_b64_tr_b16 v[232:233], v213 offset:45568
	ds_read_b64_tr_b16 v[234:235], v213 offset:46592
	ds_read_b64_tr_b16 v[236:237], v213 offset:47616
	ds_read_b64_tr_b16 v[238:239], v213 offset:48640
	s_waitcnt lgkmcnt(8)
	v_mfma_f32_32x32x16_bf16 v[50:65], v[138:141], v[156:159], v[50:65]
	v_add_f32_e32 v164, v78, v164
	v_add_f32_e32 v164, v79, v164
	v_add_f32_e32 v164, v80, v164
	v_add_f32_e32 v154, v81, v164
	v_mov_b32_e32 v155, v154
	v_mfma_f32_32x32x16_bf16 v[50:65], v[142:145], v[160:163], v[50:65]
	v_cvt_pk_bf16_f32 v66, v66, v67
	v_cvt_pk_bf16_f32 v67, v68, v69
	v_cvt_pk_bf16_f32 v68, v70, v71
	v_cvt_pk_bf16_f32 v69, v72, v73
	v_cvt_pk_bf16_f32 v70, v74, v75
	v_cvt_pk_bf16_f32 v71, v76, v77
	v_cvt_pk_bf16_f32 v72, v78, v79
	v_cvt_pk_bf16_f32 v73, v80, v81
	v_permlane32_swap_b32_e32 v154, v155
	v_mfma_f32_32x32x16_bf16 v[50:65], v[146:149], v[66:69], v[50:65]
	s_add_i32 s8, s13, -1
	s_cmp_lt_u32 s8, s31
	s_cselect_b32 s9, 0, s31
	s_cselect_b32 s35, s12, s29
	s_lshl_b32 s9, s9, 6
	s_sub_i32 s9, s35, s9
	s_lshl_b32 s52, s9, 8
	s_add_i32 s52, s52, -16384
	v_mfma_f32_32x32x16_bf16 v[50:65], v[150:153], v[70:73], v[50:65]
	v_add_u32_e32 v126, s52, v137
	global_load_dwordx4 v[130:133], v126, s[42:43]
	global_load_dwordx4 v[126:129], v126, s[44:45]
	s_waitcnt lgkmcnt(0)
	v_mfma_f32_32x32x16_bf16 v[34:49], v[224:227], v[156:159], v[34:49]
	s_waitcnt vmcnt(2)
	ds_write_b128 v187, v[118:121] offset:20480
	ds_write_b128 v214, v[122:125] offset:32768
	v_exp_f32_e32 v168, v98
	v_exp_f32_e32 v169, v99
	v_mfma_f32_32x32x16_bf16 v[34:49], v[228:231], v[160:163], v[34:49]
	v_exp_f32_e32 v170, v100
	v_exp_f32_e32 v171, v101
	v_exp_f32_e32 v172, v102
	v_exp_f32_e32 v173, v103
	v_mfma_f32_32x32x16_bf16 v[34:49], v[232:235], v[66:69], v[34:49]
	v_exp_f32_e32 v174, v104
	v_exp_f32_e32 v175, v105
	v_exp_f32_e32 v176, v106
	v_exp_f32_e32 v177, v107
	v_exp_f32_e32 v178, v108
	v_mfma_f32_32x32x16_bf16 v[34:49], v[236:239], v[70:73], v[34:49]
	v_exp_f32_e32 v179, v109
	v_exp_f32_e32 v180, v110
	v_exp_f32_e32 v181, v111
	v_exp_f32_e32 v182, v112
	v_exp_f32_e32 v183, v113
	s_waitcnt lgkmcnt(0)
	s_barrier
; #define LAS __attribute__((address_space(3)))
; __device__ __forceinline__ void finishSM(f32x16& p0, f32x16& p1, float alpha, float& l_reg, bf16x8& pa0, bf16x8& pa1, bf16x8& pa2, bf16x8& pa3) {
; #pragma unroll
;     for (int r = 0; r < 16; ++r) p1[r] = EXP_PROBE ? fmaf(p1[r], 0.001f, 1.f) : __builtin_amdgcn_exp2f(p1[r]);
;     float ps = 0.f;
; #pragma unroll
;     for (int r = 0; r < 16; ++r) ps += p0[r];
; #pragma unroll
;     for (int r = 0; r < 16; ++r) ps += p1[r];
;     { auto rr = __builtin_amdgcn_permlane32_swap(__float_as_uint(ps), __float_as_uint(ps), false, false);
;       ps = __uint_as_float(rr[0]) + __uint_as_float(rr[1]); }
;     l_reg = l_reg * alpha + ps;
;     ATT_PKN(p0, 0, pa0); ATT_PKN(p0, 8, pa1); ATT_PKN(p1, 0, pa2); ATT_PKN(p1, 8, pa3);
; }
; template <int DQK> __device__ __forceinline__ void qkt(f32x16& p0, f32x16& p1, const LAS char* buf, const bf16x8* qr, int r32, int hi, const f32x16& negm) {
; #pragma unroll
;     for (int d0 = 0; d0 < 4; ++d0) { const int ch = d0 * 2 + hi;
;         const bf16x8 b0 = *(const LAS bf16x8*)(buf + B_KN + swz64(r32, ch));
;         const bf16x8 b1 = *(const LAS bf16x8*)(buf + B_KN + swz64(32 + r32, ch));
;         p0 = __builtin_amdgcn_mfma_f32_32x32x16_bf16(b0, qr[d0], d0 == 0 ? negm : p0, 0, 0, 0);
;         p1 = __builtin_amdgcn_mfma_f32_32x32x16_bf16(b1, qr[d0], d0 == 0 ? negm : p1, 0, 0, 0); }
; template <bool FIXM> __device__ __forceinline__ void pv_psm(f32x16& o0, f32x16& o1, unsigned vb, bf16x8 pa0, bf16x8 pa1, bf16x8 pa2, bf16x8 pa3,
;                                        f32x16& p0, f32x16& p1, float& m_reg, f32x16& negm, float& alpha) {
;     { const s16x4 l0 = tr_read<v_rd_off(0, 0, 0)>(vb), h0 = tr_read<v_rd_off(0, 0, 1)>(vb), l1 = tr_read<v_rd_off(0, 1, 0)>(vb), h1 = tr_read<v_rd_off(0, 1, 1)>(vb);
;       const s16x4 l2 = tr_read<v_rd_off(0, 2, 0)>(vb), h2 = tr_read<v_rd_off(0, 2, 1)>(vb), l3 = tr_read<v_rd_off(0, 3, 0)>(vb), h3 = tr_read<v_rd_off(0, 3, 1)>(vb);
;       float pmax = 0.f; SBAR(); if (!FIXM) pmax = psm_max(p0, p1); else { _Pragma("unroll") for (int r = 0; r < 8; ++r) p0[r] = __builtin_amdgcn_exp2f(p0[r]); } SBAR();
;       asm volatile("s_waitcnt lgkmcnt(0)" ::: "memory"); SBAR();
;       o0 = __builtin_amdgcn_mfma_f32_32x32x16_bf16(ATT_PK(l0, h0), pa0, o0, 0, 0, 0);
;       o0 = __builtin_amdgcn_mfma_f32_32x32x16_bf16(ATT_PK(l1, h1), pa1, o0, 0, 0, 0);
	ds_read_b128 v[224:227], v223 offset:20480
	ds_read_b128 v[228:231], v223 offset:24576
	ds_read_b128 v[232:235], v252 offset:20480
	ds_read_b128 v[236:239], v252 offset:24576
	ds_read_b128 v[240:243], v253 offset:20480
	ds_read_b128 v[244:247], v253 offset:24576
	ds_read_b128 v[248:251], v2 offset:20480
	v_exp_f32_e32 v82, v82
	v_exp_f32_e32 v83, v83
	v_exp_f32_e32 v84, v84
	v_exp_f32_e32 v85, v85
	v_exp_f32_e32 v86, v86
	v_exp_f32_e32 v87, v87
	v_exp_f32_e32 v88, v88
	v_exp_f32_e32 v89, v89
	s_waitcnt lgkmcnt(6)
	v_mfma_f32_32x32x16_bf16 v[98:113], v[224:227], v[114:117], v[18:33]
	ds_read_b128 v[224:227], v2 offset:24576
	v_exp_f32_e32 v90, v90
	v_exp_f32_e32 v91, v91
	v_exp_f32_e32 v92, v92
	v_cvt_pk_bf16_f32 v156, v168, v169
	v_cvt_pk_bf16_f32 v157, v170, v171
	v_add_f32_e32 v164, 0, v168
	v_add_f32_e32 v164, v169, v164
	v_add_f32_e32 v164, v170, v164
	s_waitcnt lgkmcnt(6)
	v_mfma_f32_32x32x16_bf16 v[66:81], v[228:231], v[114:117], v[18:33]
	v_exp_f32_e32 v93, v93
	v_exp_f32_e32 v94, v94
	v_exp_f32_e32 v95, v95
	v_cvt_pk_bf16_f32 v158, v172, v173
	v_cvt_pk_bf16_f32 v159, v174, v175
	v_add_f32_e32 v164, v171, v164
	v_add_f32_e32 v164, v172, v164
	v_add_f32_e32 v164, v173, v164
	s_waitcnt lgkmcnt(5)
	v_mfma_f32_32x32x16_bf16 v[98:113], v[232:235], v[12:15], v[98:113]
	v_exp_f32_e32 v96, v96
	v_exp_f32_e32 v97, v97
	v_cvt_pk_bf16_f32 v160, v176, v177
	v_cvt_pk_bf16_f32 v161, v178, v179
	v_cvt_pk_bf16_f32 v162, v180, v181
	v_cvt_pk_bf16_f32 v163, v182, v183
	v_add_f32_e32 v164, v174, v164
	v_add_f32_e32 v164, v175, v164
	v_add_f32_e32 v164, v176, v164
	s_waitcnt lgkmcnt(4)
	v_mfma_f32_32x32x16_bf16 v[66:81], v[236:239], v[12:15], v[66:81]
	v_add_f32_e32 v164, v177, v164
	v_add_f32_e32 v164, v178, v164
	v_add_f32_e32 v164, v179, v164
	v_add_f32_e32 v164, v180, v164
	v_add_f32_e32 v164, v181, v164
	v_add_f32_e32 v164, v182, v164
	v_add_f32_e32 v164, v183, v164
	s_waitcnt lgkmcnt(3)
	v_mfma_f32_32x32x16_bf16 v[98:113], v[240:243], v[8:11], v[98:113]
	ds_read_b64_tr_b16 v[168:169], v213 offset:0
	ds_read_b64_tr_b16 v[170:171], v213 offset:1024
	ds_read_b64_tr_b16 v[172:173], v213 offset:2048
	ds_read_b64_tr_b16 v[174:175], v213 offset:3072
	v_add_f32_e32 v164, v82, v164
	v_add_f32_e32 v164, v83, v164
	v_add_f32_e32 v164, v84, v164
	v_add_f32_e32 v164, v85, v164
	s_waitcnt lgkmcnt(6)
	v_mfma_f32_32x32x16_bf16 v[66:81], v[244:247], v[8:11], v[66:81]
	ds_read_b64_tr_b16 v[176:177], v213 offset:4096
	ds_read_b64_tr_b16 v[178:179], v213 offset:5120
	ds_read_b64_tr_b16 v[180:181], v213 offset:6144
	ds_read_b64_tr_b16 v[182:183], v213 offset:7168
	v_add_f32_e32 v164, v86, v164
	v_add_f32_e32 v164, v87, v164
	v_add_f32_e32 v164, v88, v164
	v_add_f32_e32 v164, v89, v164
	s_waitcnt lgkmcnt(9)
	v_mfma_f32_32x32x16_bf16 v[98:113], v[248:251], v[4:7], v[98:113]
	v_add_f32_e32 v164, v90, v164
	v_add_f32_e32 v164, v91, v164
	v_add_f32_e32 v164, v92, v164
	v_add_f32_e32 v164, v93, v164
	s_waitcnt lgkmcnt(8)
	v_mfma_f32_32x32x16_bf16 v[66:81], v[224:227], v[4:7], v[66:81]
	ds_read_b64_tr_b16 v[224:225], v213 offset:512
	ds_read_b64_tr_b16 v[226:227], v213 offset:1536
	ds_read_b64_tr_b16 v[228:229], v213 offset:2560
	ds_read_b64_tr_b16 v[230:231], v213 offset:3584
	ds_read_b64_tr_b16 v[232:233], v213 offset:4608
	ds_read_b64_tr_b16 v[234:235], v213 offset:5632
	ds_read_b64_tr_b16 v[236:237], v213 offset:6656
	ds_read_b64_tr_b16 v[238:239], v213 offset:7680
	s_waitcnt lgkmcnt(8)
	v_mfma_f32_32x32x16_bf16 v[50:65], v[168:171], v[156:159], v[50:65]
	v_add_f32_e32 v164, v94, v164
	v_add_f32_e32 v164, v95, v164
	v_add_f32_e32 v164, v96, v164
	v_add_f32_e32 v164, v97, v164
	v_mov_b32_e32 v165, v164
	v_mfma_f32_32x32x16_bf16 v[50:65], v[172:175], v[160:163], v[50:65]
	v_cvt_pk_bf16_f32 v82, v82, v83
	v_cvt_pk_bf16_f32 v83, v84, v85
	v_cvt_pk_bf16_f32 v84, v86, v87
	v_cvt_pk_bf16_f32 v85, v88, v89
	v_cvt_pk_bf16_f32 v86, v90, v91
	v_cvt_pk_bf16_f32 v87, v92, v93
	v_cvt_pk_bf16_f32 v88, v94, v95
	v_cvt_pk_bf16_f32 v89, v96, v97
	v_permlane32_swap_b32_e32 v164, v165
	v_mfma_f32_32x32x16_bf16 v[50:65], v[176:179], v[82:85], v[50:65]
	v_mfma_f32_32x32x16_bf16 v[50:65], v[180:183], v[86:89], v[50:65]
	s_cmp_ge_u32 s13, s30
	s_cbranch_scc1 .Lgqa_b_noload_1
	s_cmp_lt_u32 s13, s31
	s_cselect_b32 s9, 0, s31
	s_cselect_b32 s35, s12, s29
	s_lshl_b32 s9, s9, 6
	s_sub_i32 s9, s35, s9
	s_lshl_b32 s52, s9, 8
	v_add_u32_e32 v122, s52, v137
	global_load_dwordx4 v[118:121], v122, s[42:43]
	global_load_dwordx4 v[122:125], v122, s[44:45]
; #define LAS __attribute__((address_space(3)))
; __device__ __forceinline__ void finishSM(f32x16& p0, f32x16& p1, float alpha, float& l_reg, bf16x8& pa0, bf16x8& pa1, bf16x8& pa2, bf16x8& pa3) {
; #pragma unroll
;     for (int r = 0; r < 16; ++r) p1[r] = EXP_PROBE ? fmaf(p1[r], 0.001f, 1.f) : __builtin_amdgcn_exp2f(p1[r]);
;     float ps = 0.f;
; #pragma unroll
;     for (int r = 0; r < 16; ++r) ps += p0[r];
; #pragma unroll
;     for (int r = 0; r < 16; ++r) ps += p1[r];
;     { auto rr = __builtin_amdgcn_permlane32_swap(__float_as_uint(ps), __float_as_uint(ps), false, false);
;       ps = __uint_as_float(rr[0]) + __uint_as_float(rr[1]); }
;     l_reg = l_reg * alpha + ps;
;     ATT_PKN(p0, 0, pa0); ATT_PKN(p0, 8, pa1); ATT_PKN(p1, 0, pa2); ATT_PKN(p1, 8, pa3);
; }
; template <int DQK> __device__ __forceinline__ void qkt(f32x16& p0, f32x16& p1, const LAS char* buf, const bf16x8* qr, int r32, int hi, const f32x16& negm) {
; #pragma unroll
;     for (int d0 = 0; d0 < 4; ++d0) { const int ch = d0 * 2 + hi;
;         const bf16x8 b0 = *(const LAS bf16x8*)(buf + B_KN + swz64(r32, ch));
;         const bf16x8 b1 = *(const LAS bf16x8*)(buf + B_KN + swz64(32 + r32, ch));
;         p0 = __builtin_amdgcn_mfma_f32_32x32x16_bf16(b0, qr[d0], d0 == 0 ? negm : p0, 0, 0, 0);
;         p1 = __builtin_amdgcn_mfma_f32_32x32x16_bf16(b1, qr[d0], d0 == 0 ? negm : p1, 0, 0, 0); }
; template <bool FIXM> __device__ __forceinline__ void pv_psm(f32x16& o0, f32x16& o1, unsigned vb, bf16x8 pa0, bf16x8 pa1, bf16x8 pa2, bf16x8 pa3,
;                                        f32x16& p0, f32x16& p1, float& m_reg, f32x16& negm, float& alpha) {
;     { const s16x4 l0 = tr_read<v_rd_off(0, 0, 0)>(vb), h0 = tr_read<v_rd_off(0, 0, 1)>(vb), l1 = tr_read<v_rd_off(0, 1, 0)>(vb), h1 = tr_read<v_rd_off(0, 1, 1)>(vb);
;       const s16x4 l2 = tr_read<v_rd_off(0, 2, 0)>(vb), h2 = tr_read<v_rd_off(0, 2, 1)>(vb), l3 = tr_read<v_rd_off(0, 3, 0)>(vb), h3 = tr_read<v_rd_off(0, 3, 1)>(vb);
;       float pmax = 0.f; SBAR(); if (!FIXM) pmax = psm_max(p0, p1); else { _Pragma("unroll") for (int r = 0; r < 8; ++r) p0[r] = __builtin_amdgcn_exp2f(p0[r]); } SBAR();
;       asm volatile("s_waitcnt lgkmcnt(0)" ::: "memory"); SBAR();
;       o0 = __builtin_amdgcn_mfma_f32_32x32x16_bf16(ATT_PK(l0, h0), pa0, o0, 0, 0, 0);
;       o0 = __builtin_amdgcn_mfma_f32_32x32x16_bf16(ATT_PK(l1, h1), pa1, o0, 0, 0, 0);
.Lgqa_b_ld_done_1:
	s_waitcnt lgkmcnt(0)
	v_mfma_f32_32x32x16_bf16 v[34:49], v[224:227], v[156:159], v[34:49]
	s_waitcnt vmcnt(2)
	ds_write_b128 v187, v[130:133] offset:40960
	ds_write_b128 v214, v[126:129] offset:53248
	v_exp_f32_e32 v143, v98
	v_exp_f32_e32 v145, v99
	v_mfma_f32_32x32x16_bf16 v[34:49], v[228:231], v[160:163], v[34:49]
	v_exp_f32_e32 v141, v100
	v_exp_f32_e32 v144, v101
	v_exp_f32_e32 v139, v102
	v_exp_f32_e32 v142, v103
	v_mfma_f32_32x32x16_bf16 v[34:49], v[232:235], v[82:85], v[34:49]
	v_exp_f32_e32 v138, v104
	v_exp_f32_e32 v140, v105
	v_exp_f32_e32 v151, v106
	v_exp_f32_e32 v153, v107
	v_exp_f32_e32 v149, v108
	v_mfma_f32_32x32x16_bf16 v[34:49], v[236:239], v[86:89], v[34:49]
	v_exp_f32_e32 v152, v109
	v_exp_f32_e32 v147, v110
	v_exp_f32_e32 v150, v111
	v_exp_f32_e32 v146, v112
	v_exp_f32_e32 v148, v113
	v_add_f32_e32 v154, v154, v155
	v_add_f32_e32 v136, v136, v154
	v_add_f32_e32 v164, v164, v165
	v_add_f32_e32 v136, v136, v164
	s_add_i32 s13, s13, 2
	v_add_u32_e32 v137, 0x8000, v137
	s_cmp_lt_u32 s8, s0
	s_cbranch_scc0 .Lgqa_exit_1
	s_waitcnt lgkmcnt(0)
	s_barrier
	ds_read_b128 v[224:227], v223 offset:40960
	ds_read_b128 v[228:231], v223 offset:45056
	ds_read_b128 v[232:235], v252 offset:40960
	ds_read_b128 v[236:239], v252 offset:45056
	ds_read_b128 v[240:243], v253 offset:40960
	ds_read_b128 v[244:247], v253 offset:45056
	ds_read_b128 v[248:251], v2 offset:40960
	v_exp_f32_e32 v66, v66
	v_exp_f32_e32 v67, v67
	v_exp_f32_e32 v68, v68
	v_exp_f32_e32 v69, v69
	v_exp_f32_e32 v70, v70
	v_exp_f32_e32 v71, v71
	v_exp_f32_e32 v72, v72
	v_exp_f32_e32 v73, v73
	s_waitcnt lgkmcnt(6)
	v_mfma_f32_32x32x16_bf16 v[98:113], v[224:227], v[114:117], v[18:33]
	ds_read_b128 v[224:227], v2 offset:45056
	v_exp_f32_e32 v74, v74
	v_exp_f32_e32 v75, v75
	v_exp_f32_e32 v76, v76
	v_cvt_pk_bf16_f32 v156, v143, v145
	v_cvt_pk_bf16_f32 v157, v141, v144
	v_add_f32_e32 v164, 0, v143
	v_add_f32_e32 v164, v145, v164
	v_add_f32_e32 v164, v141, v164
	s_waitcnt lgkmcnt(6)
	v_mfma_f32_32x32x16_bf16 v[82:97], v[228:231], v[114:117], v[18:33]
	v_exp_f32_e32 v77, v77
	v_exp_f32_e32 v78, v78
	v_exp_f32_e32 v79, v79
	v_cvt_pk_bf16_f32 v158, v139, v142
	v_cvt_pk_bf16_f32 v159, v138, v140
	v_add_f32_e32 v164, v144, v164
	v_add_f32_e32 v164, v139, v164
	v_add_f32_e32 v164, v142, v164
	s_waitcnt lgkmcnt(5)
	v_mfma_f32_32x32x16_bf16 v[98:113], v[232:235], v[12:15], v[98:113]
	v_exp_f32_e32 v80, v80
	v_exp_f32_e32 v81, v81
	v_cvt_pk_bf16_f32 v160, v151, v153
	v_cvt_pk_bf16_f32 v161, v149, v152
	v_cvt_pk_bf16_f32 v162, v147, v150
	v_cvt_pk_bf16_f32 v163, v146, v148
	v_add_f32_e32 v164, v138, v164
	v_add_f32_e32 v164, v140, v164
	v_add_f32_e32 v164, v151, v164
	s_waitcnt lgkmcnt(4)
	v_mfma_f32_32x32x16_bf16 v[82:97], v[236:239], v[12:15], v[82:97]
	v_add_f32_e32 v164, v153, v164
	v_add_f32_e32 v164, v149, v164
	v_add_f32_e32 v164, v152, v164
	v_add_f32_e32 v164, v147, v164
	v_add_f32_e32 v164, v150, v164
	v_add_f32_e32 v164, v146, v164
	v_add_f32_e32 v164, v148, v164
	s_waitcnt lgkmcnt(3)
	v_mfma_f32_32x32x16_bf16 v[98:113], v[240:243], v[8:11], v[98:113]
	ds_read_b64_tr_b16 v[138:139], v213 offset:20480
	ds_read_b64_tr_b16 v[140:141], v213 offset:21504
	ds_read_b64_tr_b16 v[142:143], v213 offset:22528
	ds_read_b64_tr_b16 v[144:145], v213 offset:23552
	v_add_f32_e32 v164, v66, v164
	v_add_f32_e32 v164, v67, v164
	v_add_f32_e32 v164, v68, v164
	v_add_f32_e32 v164, v69, v164
	s_waitcnt lgkmcnt(6)
	v_mfma_f32_32x32x16_bf16 v[82:97], v[244:247], v[8:11], v[82:97]
	ds_read_b64_tr_b16 v[146:147], v213 offset:24576
	ds_read_b64_tr_b16 v[148:149], v213 offset:25600
	ds_read_b64_tr_b16 v[150:151], v213 offset:26624
	ds_read_b64_tr_b16 v[152:153], v213 offset:27648
	v_add_f32_e32 v164, v70, v164
	v_add_f32_e32 v164, v71, v164
	v_add_f32_e32 v164, v72, v164
	v_add_f32_e32 v164, v73, v164
	s_waitcnt lgkmcnt(9)
	v_mfma_f32_32x32x16_bf16 v[98:113], v[248:251], v[4:7], v[98:113]
	v_add_f32_e32 v164, v74, v164
	v_add_f32_e32 v164, v75, v164
	v_add_f32_e32 v164, v76, v164
	v_add_f32_e32 v164, v77, v164
	s_waitcnt lgkmcnt(8)
	v_mfma_f32_32x32x16_bf16 v[82:97], v[224:227], v[4:7], v[82:97]
	ds_read_b64_tr_b16 v[224:225], v213 offset:20992
	ds_read_b64_tr_b16 v[226:227], v213 offset:22016
	ds_read_b64_tr_b16 v[228:229], v213 offset:23040
	ds_read_b64_tr_b16 v[230:231], v213 offset:24064
	ds_read_b64_tr_b16 v[232:233], v213 offset:25088
	ds_read_b64_tr_b16 v[234:235], v213 offset:26112
	ds_read_b64_tr_b16 v[236:237], v213 offset:27136
	ds_read_b64_tr_b16 v[238:239], v213 offset:28160
	s_waitcnt lgkmcnt(8)
	v_mfma_f32_32x32x16_bf16 v[50:65], v[138:141], v[156:159], v[50:65]
	v_add_f32_e32 v164, v78, v164
	v_add_f32_e32 v164, v79, v164
	v_add_f32_e32 v164, v80, v164
	v_add_f32_e32 v154, v81, v164
	v_mov_b32_e32 v155, v154
	v_mfma_f32_32x32x16_bf16 v[50:65], v[142:145], v[160:163], v[50:65]
	v_cvt_pk_bf16_f32 v66, v66, v67
	v_cvt_pk_bf16_f32 v67, v68, v69
	v_cvt_pk_bf16_f32 v68, v70, v71
	v_cvt_pk_bf16_f32 v69, v72, v73
	v_cvt_pk_bf16_f32 v70, v74, v75
	v_cvt_pk_bf16_f32 v71, v76, v77
	v_cvt_pk_bf16_f32 v72, v78, v79
	v_cvt_pk_bf16_f32 v73, v80, v81
	v_permlane32_swap_b32_e32 v154, v155
	v_mfma_f32_32x32x16_bf16 v[50:65], v[146:149], v[66:69], v[50:65]
	s_add_i32 s8, s13, -1
	s_cmp_lt_u32 s8, s31
	s_cselect_b32 s9, 0, s31
	s_cselect_b32 s35, s12, s29
	s_lshl_b32 s9, s9, 6
	s_sub_i32 s9, s35, s9
	s_lshl_b32 s52, s9, 8
	s_add_i32 s52, s52, -16384
	v_mfma_f32_32x32x16_bf16 v[50:65], v[150:153], v[70:73], v[50:65]
	v_add_u32_e32 v126, s52, v137
	global_load_dwordx4 v[130:133], v126, s[42:43]
	global_load_dwordx4 v[126:129], v126, s[44:45]
	s_waitcnt lgkmcnt(0)
	v_mfma_f32_32x32x16_bf16 v[34:49], v[224:227], v[156:159], v[34:49]
	s_waitcnt vmcnt(2)
	ds_write_b128 v187, v[118:121] offset:0
	ds_write_b128 v214, v[122:125] offset:12288
	v_exp_f32_e32 v168, v98
	v_exp_f32_e32 v169, v99
	v_mfma_f32_32x32x16_bf16 v[34:49], v[228:231], v[160:163], v[34:49]
	v_exp_f32_e32 v170, v100
	v_exp_f32_e32 v171, v101
	v_exp_f32_e32 v172, v102
	v_exp_f32_e32 v173, v103
	v_mfma_f32_32x32x16_bf16 v[34:49], v[232:235], v[66:69], v[34:49]
	v_exp_f32_e32 v174, v104
	v_exp_f32_e32 v175, v105
	v_exp_f32_e32 v176, v106
	v_exp_f32_e32 v177, v107
	v_exp_f32_e32 v178, v108
	v_mfma_f32_32x32x16_bf16 v[34:49], v[236:239], v[70:73], v[34:49]
	v_exp_f32_e32 v179, v109
	v_exp_f32_e32 v180, v110
	v_exp_f32_e32 v181, v111
	v_exp_f32_e32 v182, v112
	v_exp_f32_e32 v183, v113
	s_waitcnt lgkmcnt(0)
	s_barrier
; #define LAS __attribute__((address_space(3)))
; __device__ __forceinline__ void finishSM(f32x16& p0, f32x16& p1, float alpha, float& l_reg, bf16x8& pa0, bf16x8& pa1, bf16x8& pa2, bf16x8& pa3) {
; #pragma unroll
;     for (int r = 0; r < 16; ++r) p1[r] = EXP_PROBE ? fmaf(p1[r], 0.001f, 1.f) : __builtin_amdgcn_exp2f(p1[r]);
;     float ps = 0.f;
; #pragma unroll
;     for (int r = 0; r < 16; ++r) ps += p0[r];
; #pragma unroll
;     for (int r = 0; r < 16; ++r) ps += p1[r];
;     { auto rr = __builtin_amdgcn_permlane32_swap(__float_as_uint(ps), __float_as_uint(ps), false, false);
;       ps = __uint_as_float(rr[0]) + __uint_as_float(rr[1]); }
;     l_reg = l_reg * alpha + ps;
;     ATT_PKN(p0, 0, pa0); ATT_PKN(p0, 8, pa1); ATT_PKN(p1, 0, pa2); ATT_PKN(p1, 8, pa3);
; }
; template <int DQK> __device__ __forceinline__ void qkt(f32x16& p0, f32x16& p1, const LAS char* buf, const bf16x8* qr, int r32, int hi, const f32x16& negm) {
; #pragma unroll
;     for (int d0 = 0; d0 < 4; ++d0) { const int ch = d0 * 2 + hi;
;         const bf16x8 b0 = *(const LAS bf16x8*)(buf + B_KN + swz64(r32, ch));
;         const bf16x8 b1 = *(const LAS bf16x8*)(buf + B_KN + swz64(32 + r32, ch));
;         p0 = __builtin_amdgcn_mfma_f32_32x32x16_bf16(b0, qr[d0], d0 == 0 ? negm : p0, 0, 0, 0);
;         p1 = __builtin_amdgcn_mfma_f32_32x32x16_bf16(b1, qr[d0], d0 == 0 ? negm : p1, 0, 0, 0); }
; template <bool FIXM> __device__ __forceinline__ void pv_psm(f32x16& o0, f32x16& o1, unsigned vb, bf16x8 pa0, bf16x8 pa1, bf16x8 pa2, bf16x8 pa3,
;                                        f32x16& p0, f32x16& p1, float& m_reg, f32x16& negm, float& alpha) {
;     { const s16x4 l0 = tr_read<v_rd_off(0, 0, 0)>(vb), h0 = tr_read<v_rd_off(0, 0, 1)>(vb), l1 = tr_read<v_rd_off(0, 1, 0)>(vb), h1 = tr_read<v_rd_off(0, 1, 1)>(vb);
;       const s16x4 l2 = tr_read<v_rd_off(0, 2, 0)>(vb), h2 = tr_read<v_rd_off(0, 2, 1)>(vb), l3 = tr_read<v_rd_off(0, 3, 0)>(vb), h3 = tr_read<v_rd_off(0, 3, 1)>(vb);
;       float pmax = 0.f; SBAR(); if (!FIXM) pmax = psm_max(p0, p1); else { _Pragma("unroll") for (int r = 0; r < 8; ++r) p0[r] = __builtin_amdgcn_exp2f(p0[r]); } SBAR();
;       asm volatile("s_waitcnt lgkmcnt(0)" ::: "memory"); SBAR();
;       o0 = __builtin_amdgcn_mfma_f32_32x32x16_bf16(ATT_PK(l0, h0), pa0, o0, 0, 0, 0);
;       o0 = __builtin_amdgcn_mfma_f32_32x32x16_bf16(ATT_PK(l1, h1), pa1, o0, 0, 0, 0);
	ds_read_b128 v[224:227], v223 offset:0
	ds_read_b128 v[228:231], v223 offset:4096
	ds_read_b128 v[232:235], v252 offset:0
	ds_read_b128 v[236:239], v252 offset:4096
	ds_read_b128 v[240:243], v253 offset:0
	ds_read_b128 v[244:247], v253 offset:4096
	ds_read_b128 v[248:251], v2 offset:0
	v_exp_f32_e32 v82, v82
	v_exp_f32_e32 v83, v83
	v_exp_f32_e32 v84, v84
	v_exp_f32_e32 v85, v85
	v_exp_f32_e32 v86, v86
	v_exp_f32_e32 v87, v87
	v_exp_f32_e32 v88, v88
	v_exp_f32_e32 v89, v89
	s_waitcnt lgkmcnt(6)
	v_mfma_f32_32x32x16_bf16 v[98:113], v[224:227], v[114:117], v[18:33]
	ds_read_b128 v[224:227], v2 offset:4096
	v_exp_f32_e32 v90, v90
	v_exp_f32_e32 v91, v91
	v_exp_f32_e32 v92, v92
	v_cvt_pk_bf16_f32 v156, v168, v169
	v_cvt_pk_bf16_f32 v157, v170, v171
	v_add_f32_e32 v164, 0, v168
	v_add_f32_e32 v164, v169, v164
	v_add_f32_e32 v164, v170, v164
	s_waitcnt lgkmcnt(6)
	v_mfma_f32_32x32x16_bf16 v[66:81], v[228:231], v[114:117], v[18:33]
	v_exp_f32_e32 v93, v93
	v_exp_f32_e32 v94, v94
	v_exp_f32_e32 v95, v95
	v_cvt_pk_bf16_f32 v158, v172, v173
	v_cvt_pk_bf16_f32 v159, v174, v175
	v_add_f32_e32 v164, v171, v164
	v_add_f32_e32 v164, v172, v164
	v_add_f32_e32 v164, v173, v164
	s_waitcnt lgkmcnt(5)
	v_mfma_f32_32x32x16_bf16 v[98:113], v[232:235], v[12:15], v[98:113]
	v_exp_f32_e32 v96, v96
	v_exp_f32_e32 v97, v97
	v_cvt_pk_bf16_f32 v160, v176, v177
	v_cvt_pk_bf16_f32 v161, v178, v179
	v_cvt_pk_bf16_f32 v162, v180, v181
	v_cvt_pk_bf16_f32 v163, v182, v183
	v_add_f32_e32 v164, v174, v164
	v_add_f32_e32 v164, v175, v164
	v_add_f32_e32 v164, v176, v164
	s_waitcnt lgkmcnt(4)
	v_mfma_f32_32x32x16_bf16 v[66:81], v[236:239], v[12:15], v[66:81]
	v_add_f32_e32 v164, v177, v164
	v_add_f32_e32 v164, v178, v164
	v_add_f32_e32 v164, v179, v164
	v_add_f32_e32 v164, v180, v164
	v_add_f32_e32 v164, v181, v164
	v_add_f32_e32 v164, v182, v164
	v_add_f32_e32 v164, v183, v164
	s_waitcnt lgkmcnt(3)
	v_mfma_f32_32x32x16_bf16 v[98:113], v[240:243], v[8:11], v[98:113]
	ds_read_b64_tr_b16 v[168:169], v213 offset:40960
	ds_read_b64_tr_b16 v[170:171], v213 offset:41984
	ds_read_b64_tr_b16 v[172:173], v213 offset:43008
	ds_read_b64_tr_b16 v[174:175], v213 offset:44032
	v_add_f32_e32 v164, v82, v164
	v_add_f32_e32 v164, v83, v164
	v_add_f32_e32 v164, v84, v164
	v_add_f32_e32 v164, v85, v164
	s_waitcnt lgkmcnt(6)
	v_mfma_f32_32x32x16_bf16 v[66:81], v[244:247], v[8:11], v[66:81]
	ds_read_b64_tr_b16 v[176:177], v213 offset:45056
	ds_read_b64_tr_b16 v[178:179], v213 offset:46080
	ds_read_b64_tr_b16 v[180:181], v213 offset:47104
	ds_read_b64_tr_b16 v[182:183], v213 offset:48128
	v_add_f32_e32 v164, v86, v164
	v_add_f32_e32 v164, v87, v164
	v_add_f32_e32 v164, v88, v164
	v_add_f32_e32 v164, v89, v164
	s_waitcnt lgkmcnt(9)
	v_mfma_f32_32x32x16_bf16 v[98:113], v[248:251], v[4:7], v[98:113]
	v_add_f32_e32 v164, v90, v164
	v_add_f32_e32 v164, v91, v164
	v_add_f32_e32 v164, v92, v164
	v_add_f32_e32 v164, v93, v164
	s_waitcnt lgkmcnt(8)
	v_mfma_f32_32x32x16_bf16 v[66:81], v[224:227], v[4:7], v[66:81]
	ds_read_b64_tr_b16 v[224:225], v213 offset:41472
	ds_read_b64_tr_b16 v[226:227], v213 offset:42496
	ds_read_b64_tr_b16 v[228:229], v213 offset:43520
	ds_read_b64_tr_b16 v[230:231], v213 offset:44544
	ds_read_b64_tr_b16 v[232:233], v213 offset:45568
	ds_read_b64_tr_b16 v[234:235], v213 offset:46592
	ds_read_b64_tr_b16 v[236:237], v213 offset:47616
	ds_read_b64_tr_b16 v[238:239], v213 offset:48640
	s_waitcnt lgkmcnt(8)
	v_mfma_f32_32x32x16_bf16 v[50:65], v[168:171], v[156:159], v[50:65]
	v_add_f32_e32 v164, v94, v164
	v_add_f32_e32 v164, v95, v164
	v_add_f32_e32 v164, v96, v164
	v_add_f32_e32 v164, v97, v164
	v_mov_b32_e32 v165, v164
	v_mfma_f32_32x32x16_bf16 v[50:65], v[172:175], v[160:163], v[50:65]
	v_cvt_pk_bf16_f32 v82, v82, v83
	v_cvt_pk_bf16_f32 v83, v84, v85
	v_cvt_pk_bf16_f32 v84, v86, v87
	v_cvt_pk_bf16_f32 v85, v88, v89
	v_cvt_pk_bf16_f32 v86, v90, v91
	v_cvt_pk_bf16_f32 v87, v92, v93
	v_cvt_pk_bf16_f32 v88, v94, v95
	v_cvt_pk_bf16_f32 v89, v96, v97
	v_permlane32_swap_b32_e32 v164, v165
	v_mfma_f32_32x32x16_bf16 v[50:65], v[176:179], v[82:85], v[50:65]
	v_mfma_f32_32x32x16_bf16 v[50:65], v[180:183], v[86:89], v[50:65]
	s_cmp_ge_u32 s13, s30
	s_cbranch_scc1 .Lgqa_b_noload_2
	s_cmp_lt_u32 s13, s31
	s_cselect_b32 s9, 0, s31
	s_cselect_b32 s35, s12, s29
	s_lshl_b32 s9, s9, 6
	s_sub_i32 s9, s35, s9
	s_lshl_b32 s52, s9, 8
	v_add_u32_e32 v122, s52, v137
	global_load_dwordx4 v[118:121], v122, s[42:43]
	global_load_dwordx4 v[122:125], v122, s[44:45]
.Lgqa_b_ld_done_2:
	s_waitcnt lgkmcnt(0)
	v_mfma_f32_32x32x16_bf16 v[34:49], v[224:227], v[156:159], v[34:49]
	s_waitcnt vmcnt(2)
	ds_write_b128 v187, v[130:133] offset:20480
	ds_write_b128 v214, v[126:129] offset:32768
	v_exp_f32_e32 v143, v98
	v_exp_f32_e32 v145, v99
	v_mfma_f32_32x32x16_bf16 v[34:49], v[228:231], v[160:163], v[34:49]
	v_exp_f32_e32 v141, v100
	v_exp_f32_e32 v144, v101
	v_exp_f32_e32 v139, v102
	v_exp_f32_e32 v142, v103
	v_mfma_f32_32x32x16_bf16 v[34:49], v[232:235], v[82:85], v[34:49]
	v_exp_f32_e32 v138, v104
	v_exp_f32_e32 v140, v105
	v_exp_f32_e32 v151, v106
	v_exp_f32_e32 v153, v107
	v_exp_f32_e32 v149, v108
	v_mfma_f32_32x32x16_bf16 v[34:49], v[236:239], v[86:89], v[34:49]
	v_exp_f32_e32 v152, v109
	v_exp_f32_e32 v147, v110
	v_exp_f32_e32 v150, v111
	v_exp_f32_e32 v146, v112
	v_exp_f32_e32 v148, v113
	v_add_f32_e32 v154, v154, v155
	v_add_f32_e32 v136, v136, v154
	v_add_f32_e32 v164, v164, v165
	v_add_f32_e32 v136, v136, v164
	s_add_i32 s13, s13, 2
	v_add_u32_e32 v137, 0x8000, v137
	s_cmp_lt_u32 s8, s0
	s_cbranch_scc1 .LBB0_497
